# row ranking shared by the block: each wave ranks only its own 4 slots (2 compares per lane + DPP sum), ranks exchanged through LDS behind one barrier; one shared rowptr/key copy
# speedup vs baseline: 1.0746x; 1.0048x over previous
.Lperm_skip0:
	s_not_b32 s2, s2
	s_add_i32 s12, s3, s2
	v_bfe_u32 v2, v0, 4, 2
	s_lshl_b32 s2, s12, 5
	v_and_b32_e32 v3, 28, v1
	s_nop 0
	v_mbcnt_lo_u32_b32 v5, -1, 0
	v_mbcnt_hi_u32_b32 v5, -1, v5
	v_min_u32_e32 v6, 32, v5
	v_add_u32_e32 v6, s2, v6
	v_min_i32_e32 v6, s4, v6
	v_lshlrev_b32_e32 v7, 2, v6
	v_lshlrev_b32_e32 v9, 2, v5
	s_waitcnt lgkmcnt(0)
	global_load_dword v8, v7, s[8:9]
	v_cmp_gt_u32_e32 vcc, 33, v5
	s_waitcnt vmcnt(0)
	s_and_saveexec_b64 s[10:11], vcc
	ds_write_b32 v9, v8 offset:16448
	s_mov_b64 exec, s[10:11]
	ds_read_b32 v10, v9 offset:16452
	v_sub_u32_e32 v11, 31, v5
	s_waitcnt lgkmcnt(0)
	v_sub_u32_e32 v10, v10, v8
	v_lshl_add_u32 v10, v10, 5, v11
	v_cmp_gt_u32_e32 vcc, 32, v5
	s_and_saveexec_b64 s[10:11], vcc
	ds_write_b32 v9, v10 offset:16608
	s_mov_b64 exec, s[10:11]
	v_bfe_u32 v6, v0, 4, 5
	v_lshlrev_b32_e32 v7, 2, v6
	v_and_b32_e32 v11, 15, v5
	v_lshlrev_b32_e32 v11, 2, v11
	v_add_u32_e32 v11, 16608, v11
	ds_read_b32 v12, v7 offset:16608
	ds_read2_b32 v[14:15], v11 offset1:16
	s_waitcnt lgkmcnt(0)
	v_sub_u32_e32 v16, v12, v14
	v_sub_u32_e32 v17, v12, v15
	v_ashrrev_i32_e32 v16, 31, v16
	v_ashrrev_i32_e32 v17, 31, v17
	v_add_u32_e32 v16, v16, v17
	v_sub_u32_e32 v17, 0, v16
	s_nop 1
	v_add_u32_dpp v17, v17, v17 quad_perm:[1,0,3,2] row_mask:0xf bank_mask:0xf
	s_nop 1
	v_add_u32_dpp v17, v17, v17 quad_perm:[2,3,0,1] row_mask:0xf bank_mask:0xf
	s_nop 1
	v_add_u32_dpp v17, v17, v17 row_half_mirror row_mask:0xf bank_mask:0xf
	s_nop 1
	v_add_u32_dpp v17, v17, v17 row_mirror row_mask:0xf bank_mask:0xf
	v_and_b32_e32 v16, 15, v5
	v_lshlrev_b32_e32 v17, 2, v17
	v_cmp_eq_u32_e32 vcc, 0, v16
	s_and_saveexec_b64 s[10:11], vcc
	ds_write_b32 v17, v6 offset:16768
	s_mov_b64 exec, s[10:11]
	s_waitcnt lgkmcnt(0)
	s_barrier
	ds_read_b32 v12, v7 offset:16768
	s_waitcnt lgkmcnt(0)
	v_add_u32_e32 v98, s2, v12
	v_lshlrev_b32_e32 v12, 2, v12
	ds_read_b32 v4, v12 offset:16448
	ds_read_b32 v16, v12 offset:16452
	v_ashrrev_i32_e32 v99, 31, v98
	v_mov_b32_e32 v2, 0
	s_waitcnt lgkmcnt(0)
	v_sub_u32_e32 v101, v16, v4
	v_cmp_gt_i32_e64 s[2:3], s4, v98
	s_mov_b64 s[4:5], exec
	s_nop 1
	v_cndmask_b32_e64 v4, 0, v4, s[2:3]
	v_cndmask_b32_e64 v101, 0, v101, s[2:3]

	.amdhsa_kernel _Z6k_spmmILb0ELi0EEvPKiPK15HIP_vector_typeIiLj2EEPKvPKfPKDF16_S9_S9_iPfPDF16_PhSC_PKhS9_SG_S9_S9_i
		.amdhsa_group_segment_fixed_size 16960
		.amdhsa_private_segment_fixed_size 0
		.amdhsa_kernarg_size 400
		.amdhsa_user_sgpr_count 2
		.amdhsa_user_sgpr_dispatch_ptr 0
		.amdhsa_user_sgpr_queue_ptr 0
		.amdhsa_user_sgpr_kernarg_segment_ptr 1
		.amdhsa_user_sgpr_dispatch_id 0
		.amdhsa_user_sgpr_kernarg_preload_length 0
		.amdhsa_user_sgpr_kernarg_preload_offset 0
		.amdhsa_user_sgpr_private_segment_size 0
		.amdhsa_uses_dynamic_stack 0
		.amdhsa_enable_private_segment 0
		.amdhsa_system_sgpr_workgroup_id_x 1
		.amdhsa_system_sgpr_workgroup_id_y 0
		.amdhsa_system_sgpr_workgroup_id_z 0
		.amdhsa_system_sgpr_workgroup_info 0
		.amdhsa_system_vgpr_workitem_id 0
		.amdhsa_next_free_vgpr 128
		.amdhsa_next_free_sgpr 50
		.amdhsa_accum_offset 128
		.amdhsa_reserve_vcc 1
		.amdhsa_float_round_mode_32 0
		.amdhsa_float_round_mode_16_64 0
		.amdhsa_float_denorm_mode_32 3
		.amdhsa_float_denorm_mode_16_64 3
		.amdhsa_dx10_clamp 1
		.amdhsa_ieee_mode 1
		.amdhsa_fp16_overflow 0
		.amdhsa_tg_split 0
		.amdhsa_exception_fp_ieee_invalid_op 0
		.amdhsa_exception_fp_denorm_src 0
		.amdhsa_exception_fp_ieee_div_zero 0
		.amdhsa_exception_fp_ieee_overflow 0
		.amdhsa_exception_fp_ieee_underflow 0
		.amdhsa_exception_fp_ieee_inexact 0
		.amdhsa_exception_int_div_zero 0
	.end_amdhsa_kernel

_Z6k_spmmILb1ELi1EEvPKiPK15HIP_vector_typeIiLj2EEPKvPKfPKDF16_S9_S9_iPfPDF16_PhSC_PKhS9_SG_S9_S9_i:
	s_load_dword s3, s[0:1], 0x90
	s_load_dwordx2 s[40:41], s[0:1], 0x10
	s_load_dwordx2 s[42:43], s[0:1], 0x50
	s_load_dwordx2 s[44:45], s[0:1], 0x20
	s_load_dwordx2 s[8:9], s[0:1], 0x0
	s_load_dwordx2 s[14:15], s[0:1], 0x8
	s_load_dword s4, s[0:1], 0x38
	s_not_b32 s2, s2
	v_lshrrev_b32_e32 v2, 4, v0
	s_waitcnt lgkmcnt(0)
	s_add_i32 s6, s3, s2
	v_bfe_u32 v1, v0, 4, 2
	s_lshl_b32 s2, s6, 5
	v_and_b32_e32 v2, 28, v2
	s_nop 0
	v_mbcnt_lo_u32_b32 v5, -1, 0
	v_mbcnt_hi_u32_b32 v5, -1, v5
	v_min_u32_e32 v6, 32, v5
	v_add_u32_e32 v6, s2, v6
	v_min_i32_e32 v6, s4, v6
	v_lshlrev_b32_e32 v7, 2, v6
	v_lshlrev_b32_e32 v9, 2, v5
	s_waitcnt lgkmcnt(0)
	global_load_dword v8, v7, s[8:9]
	v_cmp_gt_u32_e32 vcc, 33, v5
	s_waitcnt vmcnt(0)
	s_and_saveexec_b64 s[10:11], vcc
	ds_write_b32 v9, v8 offset:16448
	s_mov_b64 exec, s[10:11]
	ds_read_b32 v10, v9 offset:16452
	v_sub_u32_e32 v11, 31, v5
	s_waitcnt lgkmcnt(0)
	v_sub_u32_e32 v10, v10, v8
	v_lshl_add_u32 v10, v10, 5, v11
	v_cmp_gt_u32_e32 vcc, 32, v5
	s_and_saveexec_b64 s[10:11], vcc
	ds_write_b32 v9, v10 offset:16608
	s_mov_b64 exec, s[10:11]
	v_bfe_u32 v6, v0, 4, 5
	v_lshlrev_b32_e32 v7, 2, v6
	v_and_b32_e32 v11, 15, v5
	v_lshlrev_b32_e32 v11, 2, v11
	v_add_u32_e32 v11, 16608, v11
	ds_read_b32 v12, v7 offset:16608
	ds_read2_b32 v[14:15], v11 offset1:16
	s_waitcnt lgkmcnt(0)
	v_sub_u32_e32 v16, v12, v14
	v_sub_u32_e32 v17, v12, v15
	v_ashrrev_i32_e32 v16, 31, v16
	v_ashrrev_i32_e32 v17, 31, v17
	v_add_u32_e32 v16, v16, v17
	v_sub_u32_e32 v17, 0, v16
	s_nop 1
	v_add_u32_dpp v17, v17, v17 quad_perm:[1,0,3,2] row_mask:0xf bank_mask:0xf
	s_nop 1
	v_add_u32_dpp v17, v17, v17 quad_perm:[2,3,0,1] row_mask:0xf bank_mask:0xf
	s_nop 1
	v_add_u32_dpp v17, v17, v17 row_half_mirror row_mask:0xf bank_mask:0xf
	s_nop 1
	v_add_u32_dpp v17, v17, v17 row_mirror row_mask:0xf bank_mask:0xf
	v_and_b32_e32 v16, 15, v5
	v_lshlrev_b32_e32 v17, 2, v17
	v_cmp_eq_u32_e32 vcc, 0, v16
	s_and_saveexec_b64 s[10:11], vcc
	ds_write_b32 v17, v6 offset:16768
	s_mov_b64 exec, s[10:11]
	s_waitcnt lgkmcnt(0)
	s_barrier
	ds_read_b32 v12, v7 offset:16768
	s_waitcnt lgkmcnt(0)
	v_add_u32_e32 v18, s2, v12
	v_lshlrev_b32_e32 v12, 2, v12
	ds_read_b32 v4, v12 offset:16448
	ds_read_b32 v16, v12 offset:16452
	v_ashrrev_i32_e32 v19, 31, v18
	v_mov_b32_e32 v2, 0
	s_waitcnt lgkmcnt(0)
	v_sub_u32_e32 v55, v16, v4
	v_cmp_gt_i32_e64 s[2:3], s4, v18
	s_mov_b64 s[4:5], exec
	s_nop 1
	v_cndmask_b32_e64 v4, 0, v4, s[2:3]
	v_cndmask_b32_e64 v55, 0, v55, s[2:3]

	.amdhsa_kernel _Z6k_spmmILb1ELi1EEvPKiPK15HIP_vector_typeIiLj2EEPKvPKfPKDF16_S9_S9_iPfPDF16_PhSC_PKhS9_SG_S9_S9_i
		.amdhsa_group_segment_fixed_size 16960
		.amdhsa_private_segment_fixed_size 0
		.amdhsa_kernarg_size 400
		.amdhsa_user_sgpr_count 2
		.amdhsa_user_sgpr_dispatch_ptr 0
		.amdhsa_user_sgpr_queue_ptr 0
		.amdhsa_user_sgpr_kernarg_segment_ptr 1
		.amdhsa_user_sgpr_dispatch_id 0
		.amdhsa_user_sgpr_kernarg_preload_length 0
		.amdhsa_user_sgpr_kernarg_preload_offset 0
		.amdhsa_user_sgpr_private_segment_size 0
		.amdhsa_uses_dynamic_stack 0
		.amdhsa_enable_private_segment 0
		.amdhsa_system_sgpr_workgroup_id_x 1
		.amdhsa_system_sgpr_workgroup_id_y 0
		.amdhsa_system_sgpr_workgroup_id_z 0
		.amdhsa_system_sgpr_workgroup_info 0
		.amdhsa_system_vgpr_workitem_id 0
		.amdhsa_next_free_vgpr 64
		.amdhsa_next_free_sgpr 46
		.amdhsa_accum_offset 64
		.amdhsa_reserve_vcc 1
		.amdhsa_float_round_mode_32 0
		.amdhsa_float_round_mode_16_64 0
		.amdhsa_float_denorm_mode_32 3
		.amdhsa_float_denorm_mode_16_64 3
		.amdhsa_dx10_clamp 1
		.amdhsa_ieee_mode 1
		.amdhsa_fp16_overflow 0
		.amdhsa_tg_split 0
		.amdhsa_exception_fp_ieee_invalid_op 0
		.amdhsa_exception_fp_denorm_src 0
		.amdhsa_exception_fp_ieee_div_zero 0
		.amdhsa_exception_fp_ieee_overflow 0
		.amdhsa_exception_fp_ieee_underflow 0
		.amdhsa_exception_fp_ieee_inexact 0
		.amdhsa_exception_int_div_zero 0
	.end_amdhsa_kernel

_Z6k_spmmILb1ELi2EEvPKiPK15HIP_vector_typeIiLj2EEPKvPKfPKDF16_S9_S9_iPfPDF16_PhSC_PKhS9_SG_S9_S9_i:
	s_load_dword s3, s[0:1], 0x90
	s_load_dwordx2 s[40:41], s[0:1], 0x10
	s_load_dwordx2 s[42:43], s[0:1], 0x70
	s_load_dwordx2 s[44:45], s[0:1], 0x60
	s_load_dwordx4 s[48:51], s[0:1], 0x40
	s_load_dwordx2 s[52:53], s[0:1], 0x20
	s_load_dwordx2 s[8:9], s[0:1], 0x0
	s_load_dwordx2 s[6:7], s[0:1], 0x8
	s_load_dword s4, s[0:1], 0x38
	v_lshrrev_b32_e32 v1, 4, v0
	s_not_b32 s2, s2
	s_waitcnt lgkmcnt(0)
	s_add_i32 s16, s3, s2
	v_and_b32_e32 v2, 28, v1
	v_lshl_or_b32 v50, s16, 5, v2
	s_lshl_b32 s5, s16, 5
	s_nop 0
	v_mbcnt_lo_u32_b32 v20, -1, 0
	v_mbcnt_hi_u32_b32 v20, -1, v20
	v_min_u32_e32 v21, 32, v20
	v_add_u32_e32 v21, s5, v21
	v_min_i32_e32 v21, s4, v21
	v_lshlrev_b32_e32 v22, 2, v21
	v_lshlrev_b32_e32 v24, 2, v20
	s_waitcnt lgkmcnt(0)
	global_load_dword v23, v22, s[8:9]
	v_cmp_gt_u32_e32 vcc, 33, v20
	s_waitcnt vmcnt(0)
	s_and_saveexec_b64 s[10:11], vcc
	ds_write_b32 v24, v23 offset:16384
	s_mov_b64 exec, s[10:11]
	ds_read_b32 v25, v24 offset:16388
	v_sub_u32_e32 v26, 31, v20
	s_waitcnt lgkmcnt(0)
	v_sub_u32_e32 v25, v25, v23
	v_lshl_add_u32 v25, v25, 5, v26
	v_cmp_gt_u32_e32 vcc, 32, v20
	s_and_saveexec_b64 s[10:11], vcc
	ds_write_b32 v24, v25 offset:16544
	s_mov_b64 exec, s[10:11]
	v_bfe_u32 v21, v0, 4, 5
	v_lshlrev_b32_e32 v22, 2, v21
	v_and_b32_e32 v26, 15, v20
	v_lshlrev_b32_e32 v26, 2, v26
	v_add_u32_e32 v26, 16544, v26
	ds_read_b32 v27, v22 offset:16544
	ds_read2_b32 v[28:29], v26 offset1:16
	s_waitcnt lgkmcnt(0)
	v_sub_u32_e32 v30, v27, v28
	v_sub_u32_e32 v31, v27, v29
	v_ashrrev_i32_e32 v30, 31, v30
	v_ashrrev_i32_e32 v31, 31, v31
	v_add_u32_e32 v30, v30, v31
	v_sub_u32_e32 v31, 0, v30
	s_nop 1
	v_add_u32_dpp v31, v31, v31 quad_perm:[1,0,3,2] row_mask:0xf bank_mask:0xf
	s_nop 1
	v_add_u32_dpp v31, v31, v31 quad_perm:[2,3,0,1] row_mask:0xf bank_mask:0xf
	s_nop 1
	v_add_u32_dpp v31, v31, v31 row_half_mirror row_mask:0xf bank_mask:0xf
	s_nop 1
	v_add_u32_dpp v31, v31, v31 row_mirror row_mask:0xf bank_mask:0xf
	v_and_b32_e32 v30, 15, v20
	v_lshlrev_b32_e32 v31, 2, v31
	v_cmp_eq_u32_e32 vcc, 0, v30
	s_and_saveexec_b64 s[10:11], vcc
	ds_write_b32 v31, v21 offset:16704
	s_mov_b64 exec, s[10:11]
	s_waitcnt lgkmcnt(0)
	s_barrier
	ds_read_b32 v27, v22 offset:16704
	s_waitcnt lgkmcnt(0)
	v_add_u32_e32 v16, s5, v27
	v_lshlrev_b32_e32 v27, 2, v27
	ds_read_b32 v4, v27 offset:16384
	ds_read_b32 v30, v27 offset:16388
	v_ashrrev_i32_e32 v17, 31, v16
	s_waitcnt lgkmcnt(0)
	v_sub_u32_e32 v52, v30, v4
	v_cmp_gt_i32_e32 vcc, s4, v16
	s_mov_b64 s[2:3], exec
	s_nop 1
	v_cndmask_b32_e32 v4, 0, v4, vcc
	v_cndmask_b32_e32 v52, 0, v52, vcc

	.amdhsa_kernel _Z6k_spmmILb1ELi2EEvPKiPK15HIP_vector_typeIiLj2EEPKvPKfPKDF16_S9_S9_iPfPDF16_PhSC_PKhS9_SG_S9_S9_i
		.amdhsa_group_segment_fixed_size 16896
		.amdhsa_private_segment_fixed_size 0
		.amdhsa_kernarg_size 400
		.amdhsa_user_sgpr_count 2
		.amdhsa_user_sgpr_dispatch_ptr 0
		.amdhsa_user_sgpr_queue_ptr 0
		.amdhsa_user_sgpr_kernarg_segment_ptr 1
		.amdhsa_user_sgpr_dispatch_id 0
		.amdhsa_user_sgpr_kernarg_preload_length 0
		.amdhsa_user_sgpr_kernarg_preload_offset 0
		.amdhsa_user_sgpr_private_segment_size 0
		.amdhsa_uses_dynamic_stack 0
		.amdhsa_enable_private_segment 0
		.amdhsa_system_sgpr_workgroup_id_x 1
		.amdhsa_system_sgpr_workgroup_id_y 0
		.amdhsa_system_sgpr_workgroup_id_z 0
		.amdhsa_system_sgpr_workgroup_info 0
		.amdhsa_system_vgpr_workitem_id 0
		.amdhsa_next_free_vgpr 64
		.amdhsa_next_free_sgpr 54
		.amdhsa_accum_offset 64
		.amdhsa_reserve_vcc 1
		.amdhsa_float_round_mode_32 0
		.amdhsa_float_round_mode_16_64 0
		.amdhsa_float_denorm_mode_32 3
		.amdhsa_float_denorm_mode_16_64 3
		.amdhsa_dx10_clamp 1
		.amdhsa_ieee_mode 1
		.amdhsa_fp16_overflow 0
		.amdhsa_tg_split 0
		.amdhsa_exception_fp_ieee_invalid_op 0
		.amdhsa_exception_fp_denorm_src 0
		.amdhsa_exception_fp_ieee_div_zero 0
		.amdhsa_exception_fp_ieee_overflow 0
		.amdhsa_exception_fp_ieee_underflow 0
		.amdhsa_exception_fp_ieee_inexact 0
		.amdhsa_exception_int_div_zero 0
	.end_amdhsa_kernel

amdhsa.kernels:
  - .agpr_count:     0
    .args:
      - .actual_access:  read_only
        .address_space:  global
        .offset:         0
        .size:           8
        .value_kind:     global_buffer
      - .actual_access:  write_only
        .address_space:  global
        .offset:         8
        .size:           8
        .value_kind:     global_buffer
      - .offset:         16
        .size:           4
        .value_kind:     by_value
      - .offset:         20
        .size:           4
        .value_kind:     by_value
    .group_segment_fixed_size: 8192
    .kernarg_segment_align: 8
    .kernarg_segment_size: 24
    .language:       OpenCL C
    .language_version:
      - 2
      - 0
    .max_flat_workgroup_size: 1024
    .name:           _Z7k_bhistPKiPiii
    .private_segment_fixed_size: 0
    .sgpr_count:     24
    .sgpr_spill_count: 0
    .symbol:         _Z7k_bhistPKiPiii.kd
    .uniform_work_group_size: 1
    .uses_dynamic_stack: false
    .vgpr_count:     50
    .vgpr_spill_count: 0
    .wavefront_size: 64
  - .agpr_count:     0
    .args:
      - .address_space:  global
        .offset:         0
        .size:           8
        .value_kind:     global_buffer
      - .actual_access:  write_only
        .address_space:  global
        .offset:         8
        .size:           8
        .value_kind:     global_buffer
      - .offset:         16
        .size:           4
        .value_kind:     by_value
      - .offset:         20
        .size:           4
        .value_kind:     by_value
      - .offset:         24
        .size:           4
        .value_kind:     by_value
      - .actual_access:  read_only
        .address_space:  global
        .offset:         32
        .size:           8
        .value_kind:     global_buffer
      - .actual_access:  read_only
        .address_space:  global
        .offset:         40
        .size:           8
        .value_kind:     global_buffer
      - .offset:         48
        .size:           4
        .value_kind:     by_value
      - .offset:         52
        .size:           4
        .value_kind:     by_value
      - .actual_access:  write_only
        .address_space:  global
        .offset:         56
        .size:           8
        .value_kind:     global_buffer
      - .actual_access:  write_only
        .address_space:  global
        .offset:         64
        .size:           8
        .value_kind:     global_buffer
      - .actual_access:  write_only
        .address_space:  global
        .offset:         72
        .size:           8
        .value_kind:     global_buffer
    .group_segment_fixed_size: 4160
    .kernarg_segment_align: 8
    .kernarg_segment_size: 80
    .language:       OpenCL C
    .language_version:
      - 2
      - 0
    .max_flat_workgroup_size: 1024
    .name:           _Z12k_bscan_prepPiS_iiiPKfS1_iiPDF16_PfS3_
    .private_segment_fixed_size: 0
    .sgpr_count:     24
    .sgpr_spill_count: 0
    .symbol:         _Z12k_bscan_prepPiS_iiiPKfS1_iiPDF16_PfS3_.kd
    .uniform_work_group_size: 1
    .uses_dynamic_stack: false
    .vgpr_count:     28
    .vgpr_spill_count: 0
    .wavefront_size: 64
  - .agpr_count:     0
    .args:
      - .actual_access:  read_only
        .address_space:  global
        .offset:         0
        .size:           8
        .value_kind:     global_buffer
      - .actual_access:  read_only
        .address_space:  global
        .offset:         8
        .size:           8
        .value_kind:     global_buffer
      - .actual_access:  read_only
        .address_space:  global
        .offset:         16
        .size:           8
        .value_kind:     global_buffer
      - .actual_access:  read_only
        .address_space:  global
        .offset:         24
        .size:           8
        .value_kind:     global_buffer
      - .actual_access:  read_only
        .address_space:  global
        .offset:         32
        .size:           8
        .value_kind:     global_buffer
      - .actual_access:  write_only
        .address_space:  global
        .offset:         40
        .size:           8
        .value_kind:     global_buffer
      - .actual_access:  write_only
        .address_space:  global
        .offset:         48
        .size:           8
        .value_kind:     global_buffer
      - .offset:         56
        .size:           4
        .value_kind:     by_value
      - .offset:         60
        .size:           4
        .value_kind:     by_value
      - .offset:         64
        .size:           4
        .value_kind:     by_value
      - .offset:         72
        .size:           4
        .value_kind:     hidden_block_count_x
      - .offset:         76
        .size:           4
        .value_kind:     hidden_block_count_y
      - .offset:         80
        .size:           4
        .value_kind:     hidden_block_count_z
      - .offset:         84
        .size:           2
        .value_kind:     hidden_group_size_x
      - .offset:         86
        .size:           2
        .value_kind:     hidden_group_size_y
      - .offset:         88
        .size:           2
        .value_kind:     hidden_group_size_z
      - .offset:         90
        .size:           2
        .value_kind:     hidden_remainder_x
      - .offset:         92
        .size:           2
        .value_kind:     hidden_remainder_y
      - .offset:         94
        .size:           2
        .value_kind:     hidden_remainder_z
      - .offset:         112
        .size:           8
        .value_kind:     hidden_global_offset_x
      - .offset:         120
        .size:           8
        .value_kind:     hidden_global_offset_y
      - .offset:         128
        .size:           8
        .value_kind:     hidden_global_offset_z
      - .offset:         136
        .size:           2
        .value_kind:     hidden_grid_dims
    .group_segment_fixed_size: 154816
    .kernarg_segment_align: 8
    .kernarg_segment_size: 328
    .language:       OpenCL C
    .language_version:
      - 2
      - 0
    .max_flat_workgroup_size: 1024
    .name:           _Z4k_l1PKiS0_PKfS0_S0_PiP15HIP_vector_typeIiLj2EEiii
    .private_segment_fixed_size: 0
    .sgpr_count:     92
    .sgpr_spill_count: 0
    .symbol:         _Z4k_l1PKiS0_PKfS0_S0_PiP15HIP_vector_typeIiLj2EEiii.kd
    .uniform_work_group_size: 1
    .uses_dynamic_stack: false
    .vgpr_count:     128
    .vgpr_spill_count: 0
    .wavefront_size: 64
  - .agpr_count:     0
    .args:
      - .actual_access:  read_only
        .address_space:  global
        .offset:         0
        .size:           8
        .value_kind:     global_buffer
      - .actual_access:  read_only
        .address_space:  global
        .offset:         8
        .size:           8
        .value_kind:     global_buffer
      - .actual_access:  write_only
        .address_space:  global
        .offset:         16
        .size:           8
        .value_kind:     global_buffer
      - .actual_access:  write_only
        .address_space:  global
        .offset:         24
        .size:           8
        .value_kind:     global_buffer
      - .offset:         32
        .size:           4
        .value_kind:     by_value
      - .offset:         36
        .size:           4
        .value_kind:     by_value
      - .offset:         40
        .size:           4
        .value_kind:     hidden_block_count_x
      - .offset:         44
        .size:           4
        .value_kind:     hidden_block_count_y
      - .offset:         48
        .size:           4
        .value_kind:     hidden_block_count_z
      - .offset:         52
        .size:           2
        .value_kind:     hidden_group_size_x
      - .offset:         54
        .size:           2
        .value_kind:     hidden_group_size_y
      - .offset:         56
        .size:           2
        .value_kind:     hidden_group_size_z
      - .offset:         58
        .size:           2
        .value_kind:     hidden_remainder_x
      - .offset:         60
        .size:           2
        .value_kind:     hidden_remainder_y
      - .offset:         62
        .size:           2
        .value_kind:     hidden_remainder_z
      - .offset:         80
        .size:           8
        .value_kind:     hidden_global_offset_x
      - .offset:         88
        .size:           8
        .value_kind:     hidden_global_offset_y
      - .offset:         96
        .size:           8
        .value_kind:     hidden_global_offset_z
      - .offset:         104
        .size:           2
        .value_kind:     hidden_grid_dims
    .group_segment_fixed_size: 80448
    .kernarg_segment_align: 8
    .kernarg_segment_size: 296
    .language:       OpenCL C
    .language_version:
      - 2
      - 0
    .max_flat_workgroup_size: 1024
    .name:           _Z4k_l2PK15HIP_vector_typeIiLj2EEPKiPiPS0_ii
    .private_segment_fixed_size: 0
    .sgpr_count:     54
    .sgpr_spill_count: 0
    .symbol:         _Z4k_l2PK15HIP_vector_typeIiLj2EEPKiPiPS0_ii.kd
    .uniform_work_group_size: 1
    .uses_dynamic_stack: false
    .vgpr_count:     64
    .vgpr_spill_count: 0
    .wavefront_size: 64
  - .agpr_count:     0
    .args:
      - .actual_access:  read_only
        .address_space:  global
        .offset:         0
        .size:           8
        .value_kind:     global_buffer
      - .actual_access:  read_only
        .address_space:  global
        .offset:         8
        .size:           8
        .value_kind:     global_buffer
      - .actual_access:  read_only
        .address_space:  global
        .offset:         16
        .size:           8
        .value_kind:     global_buffer
      - .actual_access:  read_only
        .address_space:  global
        .offset:         24
        .size:           8
        .value_kind:     global_buffer
      - .actual_access:  read_only
        .address_space:  global
        .offset:         32
        .size:           8
        .value_kind:     global_buffer
      - .actual_access:  read_only
        .address_space:  global
        .offset:         40
        .size:           8
        .value_kind:     global_buffer
      - .actual_access:  read_only
        .address_space:  global
        .offset:         48
        .size:           8
        .value_kind:     global_buffer
      - .offset:         56
        .size:           4
        .value_kind:     by_value
      - .actual_access:  read_only
        .address_space:  global
        .offset:         64
        .size:           8
        .value_kind:     global_buffer
      - .actual_access:  write_only
        .address_space:  global
        .offset:         72
        .size:           8
        .value_kind:     global_buffer
      - .actual_access:  write_only
        .address_space:  global
        .offset:         80
        .size:           8
        .value_kind:     global_buffer
      - .actual_access:  write_only
        .address_space:  global
        .offset:         88
        .size:           8
        .value_kind:     global_buffer
      - .actual_access:  read_only
        .address_space:  global
        .offset:         96
        .size:           8
        .value_kind:     global_buffer
      - .actual_access:  read_only
        .address_space:  global
        .offset:         104
        .size:           8
        .value_kind:     global_buffer
      - .actual_access:  read_only
        .address_space:  global
        .offset:         112
        .size:           8
        .value_kind:     global_buffer
      - .actual_access:  read_only
        .address_space:  global
        .offset:         120
        .size:           8
        .value_kind:     global_buffer
      - .actual_access:  read_only
        .address_space:  global
        .offset:         128
        .size:           8
        .value_kind:     global_buffer
      - .offset:         136
        .size:           4
        .value_kind:     by_value
      - .offset:         144
        .size:           4
        .value_kind:     hidden_block_count_x
      - .offset:         148
        .size:           4
        .value_kind:     hidden_block_count_y
      - .offset:         152
        .size:           4
        .value_kind:     hidden_block_count_z
      - .offset:         156
        .size:           2
        .value_kind:     hidden_group_size_x
      - .offset:         158
        .size:           2
        .value_kind:     hidden_group_size_y
      - .offset:         160
        .size:           2
        .value_kind:     hidden_group_size_z
      - .offset:         162
        .size:           2
        .value_kind:     hidden_remainder_x
      - .offset:         164
        .size:           2
        .value_kind:     hidden_remainder_y
      - .offset:         166
        .size:           2
        .value_kind:     hidden_remainder_z
      - .offset:         184
        .size:           8
        .value_kind:     hidden_global_offset_x
      - .offset:         192
        .size:           8
        .value_kind:     hidden_global_offset_y
      - .offset:         200
        .size:           8
        .value_kind:     hidden_global_offset_z
      - .offset:         208
        .size:           2
        .value_kind:     hidden_grid_dims
    .group_segment_fixed_size: 16960
    .kernarg_segment_align: 8
    .kernarg_segment_size: 400
    .language:       OpenCL C
    .language_version:
      - 2
      - 0
    .max_flat_workgroup_size: 512
    .name:           _Z6k_spmmILb0ELi0EEvPKiPK15HIP_vector_typeIiLj2EEPKvPKfPKDF16_S9_S9_iPfPDF16_PhSC_PKhS9_SG_S9_S9_i
    .private_segment_fixed_size: 0
    .sgpr_count:     56
    .sgpr_spill_count: 0
    .symbol:         _Z6k_spmmILb0ELi0EEvPKiPK15HIP_vector_typeIiLj2EEPKvPKfPKDF16_S9_S9_iPfPDF16_PhSC_PKhS9_SG_S9_S9_i.kd
    .uniform_work_group_size: 1
    .uses_dynamic_stack: false
    .vgpr_count:     128
    .vgpr_spill_count: 0
    .wavefront_size: 64
  - .agpr_count:     0
    .args:
      - .actual_access:  read_only
        .address_space:  global
        .offset:         0
        .size:           8
        .value_kind:     global_buffer
      - .actual_access:  read_only
        .address_space:  global
        .offset:         8
        .size:           8
        .value_kind:     global_buffer
      - .actual_access:  read_only
        .address_space:  global
        .offset:         16
        .size:           8
        .value_kind:     global_buffer
      - .actual_access:  read_only
        .address_space:  global
        .offset:         24
        .size:           8
        .value_kind:     global_buffer
      - .actual_access:  read_only
        .address_space:  global
        .offset:         32
        .size:           8
        .value_kind:     global_buffer
      - .actual_access:  read_only
        .address_space:  global
        .offset:         40
        .size:           8
        .value_kind:     global_buffer
      - .actual_access:  read_only
        .address_space:  global
        .offset:         48
        .size:           8
        .value_kind:     global_buffer
      - .offset:         56
        .size:           4
        .value_kind:     by_value
      - .actual_access:  read_only
        .address_space:  global
        .offset:         64
        .size:           8
        .value_kind:     global_buffer
      - .actual_access:  read_only
        .address_space:  global
        .offset:         72
        .size:           8
        .value_kind:     global_buffer
      - .actual_access:  write_only
        .address_space:  global
        .offset:         80
        .size:           8
        .value_kind:     global_buffer
      - .actual_access:  write_only
        .address_space:  global
        .offset:         88
        .size:           8
        .value_kind:     global_buffer
      - .actual_access:  read_only
        .address_space:  global
        .offset:         96
        .size:           8
        .value_kind:     global_buffer
      - .actual_access:  read_only
        .address_space:  global
        .offset:         104
        .size:           8
        .value_kind:     global_buffer
      - .actual_access:  read_only
        .address_space:  global
        .offset:         112
        .size:           8
        .value_kind:     global_buffer
      - .actual_access:  read_only
        .address_space:  global
        .offset:         120
        .size:           8
        .value_kind:     global_buffer
      - .actual_access:  read_only
        .address_space:  global
        .offset:         128
        .size:           8
        .value_kind:     global_buffer
      - .offset:         136
        .size:           4
        .value_kind:     by_value
      - .offset:         144
        .size:           4
        .value_kind:     hidden_block_count_x
      - .offset:         148
        .size:           4
        .value_kind:     hidden_block_count_y
      - .offset:         152
        .size:           4
        .value_kind:     hidden_block_count_z
      - .offset:         156
        .size:           2
        .value_kind:     hidden_group_size_x
      - .offset:         158
        .size:           2
        .value_kind:     hidden_group_size_y
      - .offset:         160
        .size:           2
        .value_kind:     hidden_group_size_z
      - .offset:         162
        .size:           2
        .value_kind:     hidden_remainder_x
      - .offset:         164
        .size:           2
        .value_kind:     hidden_remainder_y
      - .offset:         166
        .size:           2
        .value_kind:     hidden_remainder_z
      - .offset:         184
        .size:           8
        .value_kind:     hidden_global_offset_x
      - .offset:         192
        .size:           8
        .value_kind:     hidden_global_offset_y
      - .offset:         200
        .size:           8
        .value_kind:     hidden_global_offset_z
      - .offset:         208
        .size:           2
        .value_kind:     hidden_grid_dims
    .group_segment_fixed_size: 16960
    .kernarg_segment_align: 8
    .kernarg_segment_size: 400
    .language:       OpenCL C
    .language_version:
      - 2
      - 0
    .max_flat_workgroup_size: 512
    .name:           _Z6k_spmmILb1ELi1EEvPKiPK15HIP_vector_typeIiLj2EEPKvPKfPKDF16_S9_S9_iPfPDF16_PhSC_PKhS9_SG_S9_S9_i
    .private_segment_fixed_size: 0
    .sgpr_count:     52
    .sgpr_spill_count: 0
    .symbol:         _Z6k_spmmILb1ELi1EEvPKiPK15HIP_vector_typeIiLj2EEPKvPKfPKDF16_S9_S9_iPfPDF16_PhSC_PKhS9_SG_S9_S9_i.kd
    .uniform_work_group_size: 1
    .uses_dynamic_stack: false
    .vgpr_count:     64
    .vgpr_spill_count: 0
    .wavefront_size: 64
  - .agpr_count:     0
    .args:
      - .actual_access:  read_only
        .address_space:  global
        .offset:         0
        .size:           8
        .value_kind:     global_buffer
      - .actual_access:  read_only
        .address_space:  global
        .offset:         8
        .size:           8
        .value_kind:     global_buffer
      - .actual_access:  read_only
        .address_space:  global
        .offset:         16
        .size:           8
        .value_kind:     global_buffer
      - .actual_access:  read_only
        .address_space:  global
        .offset:         24
        .size:           8
        .value_kind:     global_buffer
      - .actual_access:  read_only
        .address_space:  global
        .offset:         32
        .size:           8
        .value_kind:     global_buffer
      - .actual_access:  read_only
        .address_space:  global
        .offset:         40
        .size:           8
        .value_kind:     global_buffer
      - .actual_access:  read_only
        .address_space:  global
        .offset:         48
        .size:           8
        .value_kind:     global_buffer
      - .offset:         56
        .size:           4
        .value_kind:     by_value
      - .actual_access:  write_only
        .address_space:  global
        .offset:         64
        .size:           8
        .value_kind:     global_buffer
      - .actual_access:  read_only
        .address_space:  global
        .offset:         72
        .size:           8
        .value_kind:     global_buffer
      - .actual_access:  read_only
        .address_space:  global
        .offset:         80
        .size:           8
        .value_kind:     global_buffer
      - .actual_access:  read_only
        .address_space:  global
        .offset:         88
        .size:           8
        .value_kind:     global_buffer
      - .actual_access:  read_only
        .address_space:  global
        .offset:         96
        .size:           8
        .value_kind:     global_buffer
      - .actual_access:  read_only
        .address_space:  global
        .offset:         104
        .size:           8
        .value_kind:     global_buffer
      - .actual_access:  read_only
        .address_space:  global
        .offset:         112
        .size:           8
        .value_kind:     global_buffer
      - .actual_access:  read_only
        .address_space:  global
        .offset:         120
        .size:           8
        .value_kind:     global_buffer
      - .actual_access:  read_only
        .address_space:  global
        .offset:         128
        .size:           8
        .value_kind:     global_buffer
      - .offset:         136
        .size:           4
        .value_kind:     by_value
      - .offset:         144
        .size:           4
        .value_kind:     hidden_block_count_x
      - .offset:         148
        .size:           4
        .value_kind:     hidden_block_count_y
      - .offset:         152
        .size:           4
        .value_kind:     hidden_block_count_z
      - .offset:         156
        .size:           2
        .value_kind:     hidden_group_size_x
      - .offset:         158
        .size:           2
        .value_kind:     hidden_group_size_y
      - .offset:         160
        .size:           2
        .value_kind:     hidden_group_size_z
      - .offset:         162
        .size:           2
        .value_kind:     hidden_remainder_x
      - .offset:         164
        .size:           2
        .value_kind:     hidden_remainder_y
      - .offset:         166
        .size:           2
        .value_kind:     hidden_remainder_z
      - .offset:         184
        .size:           8
        .value_kind:     hidden_global_offset_x
      - .offset:         192
        .size:           8
        .value_kind:     hidden_global_offset_y
      - .offset:         200
        .size:           8
        .value_kind:     hidden_global_offset_z
      - .offset:         208
        .size:           2
        .value_kind:     hidden_grid_dims
    .group_segment_fixed_size: 16896
    .kernarg_segment_align: 8
    .kernarg_segment_size: 400
    .language:       OpenCL C
    .language_version:
      - 2
      - 0
    .max_flat_workgroup_size: 512
    .name:           _Z6k_spmmILb1ELi2EEvPKiPK15HIP_vector_typeIiLj2EEPKvPKfPKDF16_S9_S9_iPfPDF16_PhSC_PKhS9_SG_S9_S9_i
    .private_segment_fixed_size: 0
    .sgpr_count:     60
    .sgpr_spill_count: 0
    .symbol:         _Z6k_spmmILb1ELi2EEvPKiPK15HIP_vector_typeIiLj2EEPKvPKfPKDF16_S9_S9_iPfPDF16_PhSC_PKhS9_SG_S9_S9_i.kd
    .uniform_work_group_size: 1
    .uses_dynamic_stack: false
    .vgpr_count:     64
    .vgpr_spill_count: 0
    .wavefront_size: 64
